# qkv epilogue: idx_out row written with one dwordx4 plus one dword instead of five dword stores
# speedup vs baseline: 1.0092x; 1.0092x over previous
.LBB1_46:
	s_or_b64 exec, exec, s[10:11]
	s_lshl_b32 s10, s22, 3
	v_ashrrev_i32_e32 v34, 3, v36
	v_and_or_b32 v36, v36, 7, s10
	v_mad_u32_u24 v56, v36, 7, v45
	s_and_saveexec_b64 s[10:11], s[0:1]
	s_movk_i32 s16, 0xc5
	v_mad_u32_u24 v1, v56, s16, v34
	v_cndmask_b32_e64 v1, -1, v1, s[4:5]
	v_lshlrev_b32_e32 v37, 2, v93
	ds_write_b32 v37, v1 offset:34816
	s_or_b64 exec, exec, s[10:11]
	s_and_b64 s[10:11], s[4:5], s[2:3]
	s_and_saveexec_b64 s[2:3], s[10:11]
	s_cbranch_execz .LBB1_52
	s_movk_i32 s10, 0xc5
	v_mad_u32_u24 v1, v36, s10, v34
	s_movk_i32 s10, 0xd8
	v_mov_b64_e32 v[36:37], s[8:9]
	v_cvt_f32_u32_e32 v57, v44
	v_mad_i64_i32 v[36:37], s[8:9], v1, s10, v[36:37]
	v_mul_i32_i24_e32 v1, 9, v45
	v_lshlrev_b32_e32 v38, 2, v1
	v_mov_b32_e32 v39, 0
	v_lshl_add_u64 v[36:37], v[36:37], 0, v[38:39]
	v_mov_b32_e32 v38, v57
	v_mov_b32_e32 v39, v57
	v_mov_b32_e32 v40, v57
	v_mov_b32_e32 v41, v57
	v_mov_b32_e32 v42, -16
	v_mov_b32_e32 v43, -1
	s_and_saveexec_b64 s[8:9], s[0:1]
	v_not_b32_e32 v42, 35
	global_store_dword v[36:37], v57, off offset:-20
	s_or_b64 exec, exec, s[8:9]
	v_lshl_add_u64 v[42:43], v[36:37], 0, v[42:43]
	global_store_dwordx4 v[42:43], v[38:41], off
